# attention unit epilogue row sums: the 32 serialized ds_bpermute round trips per unit also become DPP row moves
# speedup vs baseline: 1.0077x; 1.0015x over previous
.LBB0_1076:
	s_andn2_b64 vcc, exec, s[4:5]
	s_waitcnt lgkmcnt(0)
	s_barrier
	s_cbranch_vccnz .LBB0_1020
	ds_read2_b32 v[84:85], v68 offset1:32
	s_lshl_b64 s[4:5], s[90:91], 11
	s_add_u32 s4, s95, s4
	s_addc_u32 s5, s96, s5
	s_add_u32 s4, s4, s29
	s_waitcnt lgkmcnt(0)
	v_mul_f32_e32 v83, v239, v84
	v_fma_f32 v2, v2, v82, -v83
	v_mul_f32_e32 v83, v239, v85
	ds_read2_b32 v[84:85], v68 offset0:64 offset1:96
	v_fma_f32 v50, v50, v82, -v83
	ds_write2_b32 v68, v2, v50 offset1:32
	s_addc_u32 s5, s5, 0
	s_add_u32 s6, s92, s84
	s_waitcnt lgkmcnt(1)
	v_mul_f32_e32 v2, v239, v84
	v_fma_f32 v2, v34, v82, -v2
	v_mul_f32_e32 v34, v239, v85
	v_fma_f32 v18, v18, v82, -v34
	ds_read2_b32 v[82:83], v68 offset0:128 offset1:160
	ds_write2_b32 v68, v2, v18 offset0:64 offset1:96
	v_add_u32_e32 v18, 0x400, v68
	s_addc_u32 s7, s93, s85
	v_mov_b32_e32 v211, v1
	s_waitcnt lgkmcnt(1)
	v_mul_f32_e32 v2, v239, v82
	v_fma_f32 v2, v3, v81, -v2
	v_mul_f32_e32 v3, v239, v83
	v_fma_f32 v3, v51, v81, -v3
	ds_write2_b32 v68, v2, v3 offset0:128 offset1:160
	ds_read2_b32 v[2:3], v68 offset0:192 offset1:224
	v_mov_b32_e32 v213, v1
	s_waitcnt lgkmcnt(0)
	v_mul_f32_e32 v2, v239, v2
	v_mul_f32_e32 v3, v239, v3
	v_fma_f32 v2, v35, v81, -v2
	v_fma_f32 v3, v19, v81, -v3
	ds_write2_b32 v68, v2, v3 offset0:192 offset1:224
	ds_read2_b32 v[2:3], v18 offset1:32
	s_waitcnt lgkmcnt(0)
	v_mul_f32_e32 v2, v239, v2
	v_mul_f32_e32 v3, v239, v3
	v_fma_f32 v2, v4, v80, -v2
	v_fma_f32 v3, v52, v80, -v3
	ds_write2_b32 v18, v2, v3 offset1:32
	ds_read2_b32 v[2:3], v18 offset0:64 offset1:96
	v_add_u32_e32 v4, 0x1000, v68
	s_waitcnt lgkmcnt(0)
	v_mul_f32_e32 v2, v239, v2
	v_mul_f32_e32 v3, v239, v3
	v_fma_f32 v2, v36, v80, -v2
	v_fma_f32 v3, v20, v80, -v3
	ds_write2_b32 v18, v2, v3 offset0:64 offset1:96
	ds_read2_b32 v[2:3], v18 offset0:128 offset1:160
	s_waitcnt lgkmcnt(0)
	v_mul_f32_e32 v2, v239, v2
	v_mul_f32_e32 v3, v239, v3
	v_fma_f32 v2, v5, v79, -v2
	v_fma_f32 v3, v53, v79, -v3
	ds_write2_b32 v18, v2, v3 offset0:128 offset1:160
	ds_read2_b32 v[2:3], v18 offset0:192 offset1:224
	s_waitcnt lgkmcnt(0)
	v_mul_f32_e32 v2, v239, v2
	v_mul_f32_e32 v3, v239, v3
	v_fma_f32 v2, v37, v79, -v2
	v_fma_f32 v3, v21, v79, -v3
	ds_write2_b32 v18, v2, v3 offset0:192 offset1:224
	ds_read2_b32 v[2:3], v4 offset1:32
	s_waitcnt lgkmcnt(0)
	v_mul_f32_e32 v2, v239, v2
	v_mul_f32_e32 v3, v239, v3
	v_fma_f32 v2, v6, v78, -v2
	v_fma_f32 v3, v54, v78, -v3
	ds_write2_b32 v4, v2, v3 offset1:32
	ds_read2_b32 v[2:3], v4 offset0:64 offset1:96
	s_waitcnt lgkmcnt(0)
	v_mul_f32_e32 v2, v239, v2
	v_mul_f32_e32 v3, v239, v3
	v_fma_f32 v2, v38, v78, -v2
	v_fma_f32 v3, v22, v78, -v3
	ds_write2_b32 v4, v2, v3 offset0:64 offset1:96
	ds_read2_b32 v[2:3], v4 offset0:128 offset1:160
	s_waitcnt lgkmcnt(0)
	v_mul_f32_e32 v2, v239, v2
	v_mul_f32_e32 v3, v239, v3
	v_fma_f32 v2, v7, v77, -v2
	v_fma_f32 v3, v55, v77, -v3
	ds_write2_b32 v4, v2, v3 offset0:128 offset1:160
	ds_read2_b32 v[2:3], v4 offset0:192 offset1:224
	s_waitcnt lgkmcnt(0)
	v_mul_f32_e32 v2, v239, v2
	v_mul_f32_e32 v3, v239, v3
	v_fma_f32 v2, v39, v77, -v2
	v_fma_f32 v3, v23, v77, -v3
	ds_write2_b32 v4, v2, v3 offset0:192 offset1:224
	v_add_u32_e32 v4, 0x1400, v68
	ds_read2_b32 v[2:3], v4 offset1:32
	s_waitcnt lgkmcnt(0)
	v_mul_f32_e32 v2, v239, v2
	v_mul_f32_e32 v3, v239, v3
	v_fma_f32 v2, v8, v76, -v2
	v_fma_f32 v3, v56, v76, -v3
	ds_write2_b32 v4, v2, v3 offset1:32
	ds_read2_b32 v[2:3], v4 offset0:64 offset1:96
	s_waitcnt lgkmcnt(0)
	v_mul_f32_e32 v2, v239, v2
	v_mul_f32_e32 v3, v239, v3
	v_fma_f32 v2, v40, v76, -v2
	v_fma_f32 v3, v24, v76, -v3
	ds_write2_b32 v4, v2, v3 offset0:64 offset1:96
	ds_read2_b32 v[2:3], v4 offset0:128 offset1:160
	s_waitcnt lgkmcnt(0)
	v_mul_f32_e32 v2, v239, v2
	v_mul_f32_e32 v3, v239, v3
	v_fma_f32 v2, v9, v75, -v2
	v_fma_f32 v3, v57, v75, -v3
	ds_write2_b32 v4, v2, v3 offset0:128 offset1:160
	ds_read2_b32 v[2:3], v4 offset0:192 offset1:224
	s_waitcnt lgkmcnt(0)
	v_mul_f32_e32 v2, v239, v2
	v_mul_f32_e32 v3, v239, v3
	v_fma_f32 v2, v41, v75, -v2
	v_fma_f32 v3, v25, v75, -v3
	ds_write2_b32 v4, v2, v3 offset0:192 offset1:224
	v_add_u32_e32 v4, 0x2000, v68
	ds_read2_b32 v[2:3], v4 offset1:32
	s_waitcnt lgkmcnt(0)
	v_mul_f32_e32 v2, v239, v2
	v_mul_f32_e32 v3, v239, v3
	v_fma_f32 v2, v10, v74, -v2
	v_fma_f32 v3, v58, v74, -v3
	ds_write2_b32 v4, v2, v3 offset1:32
	ds_read2_b32 v[2:3], v4 offset0:64 offset1:96
	v_lshlrev_b32_e32 v10, 2, v198
	s_waitcnt lgkmcnt(0)
	v_mul_f32_e32 v2, v239, v2
	v_mul_f32_e32 v3, v239, v3
	v_fma_f32 v2, v42, v74, -v2
	v_fma_f32 v3, v26, v74, -v3
	ds_write2_b32 v4, v2, v3 offset0:64 offset1:96
	ds_read2_b32 v[2:3], v4 offset0:128 offset1:160
	s_waitcnt lgkmcnt(0)
	v_mul_f32_e32 v2, v239, v2
	v_mul_f32_e32 v3, v239, v3
	v_fma_f32 v2, v11, v73, -v2
	v_fma_f32 v3, v59, v73, -v3
	ds_write2_b32 v4, v2, v3 offset0:128 offset1:160
	ds_read2_b32 v[2:3], v4 offset0:192 offset1:224
	v_mov_b32_e32 v11, v1
	s_waitcnt lgkmcnt(0)
	v_mul_f32_e32 v2, v239, v2
	v_mul_f32_e32 v3, v239, v3
	v_fma_f32 v2, v43, v73, -v2
	v_fma_f32 v3, v27, v73, -v3
	ds_write2_b32 v4, v2, v3 offset0:192 offset1:224
	v_add_u32_e32 v4, 0x2400, v68
	ds_read2_b32 v[2:3], v4 offset1:32
	s_waitcnt lgkmcnt(0)
	v_mul_f32_e32 v2, v239, v2
	v_mul_f32_e32 v3, v239, v3
	v_fma_f32 v2, v12, v72, -v2
	v_fma_f32 v3, v60, v72, -v3
	ds_write2_b32 v4, v2, v3 offset1:32
	ds_read2_b32 v[2:3], v4 offset0:64 offset1:96
	s_waitcnt lgkmcnt(0)
	v_mul_f32_e32 v2, v239, v2
	v_mul_f32_e32 v3, v239, v3
	v_fma_f32 v2, v44, v72, -v2
	v_fma_f32 v3, v28, v72, -v3
	ds_write2_b32 v4, v2, v3 offset0:64 offset1:96
	ds_read2_b32 v[2:3], v4 offset0:128 offset1:160
	s_waitcnt lgkmcnt(0)
	v_mul_f32_e32 v2, v239, v2
	v_mul_f32_e32 v3, v239, v3
	v_fma_f32 v2, v13, v71, -v2
	v_fma_f32 v3, v61, v71, -v3
	ds_write2_b32 v4, v2, v3 offset0:128 offset1:160
	ds_read2_b32 v[2:3], v4 offset0:192 offset1:224
	s_waitcnt lgkmcnt(0)
	v_mul_f32_e32 v2, v239, v2
	v_mul_f32_e32 v3, v239, v3
	v_fma_f32 v2, v45, v71, -v2
	v_fma_f32 v3, v29, v71, -v3
	ds_write2_b32 v4, v2, v3 offset0:192 offset1:224
	v_add_u32_e32 v4, 0x3000, v68
	ds_read2_b32 v[2:3], v4 offset1:32
	s_waitcnt lgkmcnt(0)
	v_mul_f32_e32 v2, v239, v2
	v_mul_f32_e32 v3, v239, v3
	v_fma_f32 v2, v14, v70, -v2
	v_fma_f32 v3, v62, v70, -v3
	ds_write2_b32 v4, v2, v3 offset1:32
	ds_read2_b32 v[2:3], v4 offset0:64 offset1:96
	v_add3_u32 v14, s8, v249, v10
	v_add_u32_e32 v25, v14, v210
	v_add_u32_e32 v24, v14, v212
	s_waitcnt lgkmcnt(0)
	v_mul_f32_e32 v2, v239, v2
	v_mul_f32_e32 v3, v239, v3
	v_fma_f32 v2, v46, v70, -v2
	v_fma_f32 v3, v30, v70, -v3
	ds_write2_b32 v4, v2, v3 offset0:64 offset1:96
	ds_read2_b32 v[2:3], v4 offset0:128 offset1:160
	s_waitcnt lgkmcnt(0)
	v_mul_f32_e32 v2, v239, v2
	v_mul_f32_e32 v3, v239, v3
	v_fma_f32 v2, v15, v69, -v2
	v_fma_f32 v3, v63, v69, -v3
	ds_write2_b32 v4, v2, v3 offset0:128 offset1:160
	ds_read2_b32 v[2:3], v4 offset0:192 offset1:224
	s_waitcnt lgkmcnt(0)
	v_mul_f32_e32 v2, v239, v2
	v_mul_f32_e32 v3, v239, v3
	v_fma_f32 v2, v47, v69, -v2
	v_fma_f32 v3, v31, v69, -v3
	ds_write2_b32 v4, v2, v3 offset0:192 offset1:224
	v_add_u32_e32 v4, 0x3400, v68
	ds_read2_b32 v[2:3], v4 offset1:32
	s_waitcnt lgkmcnt(0)
	v_mul_f32_e32 v2, v239, v2
	v_mul_f32_e32 v3, v239, v3
	v_fma_f32 v2, v16, v67, -v2
	v_fma_f32 v3, v64, v67, -v3
	ds_write2_b32 v4, v2, v3 offset1:32
	ds_read2_b32 v[2:3], v4 offset0:64 offset1:96
	s_waitcnt lgkmcnt(0)
	v_mul_f32_e32 v2, v239, v2
	v_mul_f32_e32 v3, v239, v3
	v_fma_f32 v2, v48, v67, -v2
	v_fma_f32 v3, v32, v67, -v3
	ds_write2_b32 v4, v2, v3 offset0:64 offset1:96
	ds_read2_b32 v[2:3], v4 offset0:128 offset1:160
	s_waitcnt lgkmcnt(0)
	v_mul_f32_e32 v2, v239, v2
	v_mul_f32_e32 v3, v239, v3
	v_fma_f32 v2, v17, v66, -v2
	v_fma_f32 v3, v65, v66, -v3
	ds_write2_b32 v4, v2, v3 offset0:128 offset1:160
	ds_read2_b32 v[2:3], v4 offset0:192 offset1:224
	s_waitcnt lgkmcnt(0)
	v_mul_f32_e32 v2, v239, v2
	v_mul_f32_e32 v3, v239, v3
	v_fma_f32 v2, v49, v66, -v2
	v_fma_f32 v3, v33, v66, -v3
	ds_write2_b32 v4, v2, v3 offset0:192 offset1:224
	v_lshl_add_u64 v[2:3], s[6:7], 0, v[10:11]
	v_or_b32_e32 v10, s88, v241
	v_ashrrev_i32_e32 v11, 31, v10
	s_waitcnt lgkmcnt(0)
	v_lshl_add_u64 v[4:5], v[2:3], 0, v[210:211]
	v_lshlrev_b64 v[10:11], 11, v[10:11]
	global_load_dwordx4 v[6:9], v[4:5], off
	v_lshl_add_u64 v[10:11], s[4:5], 0, v[10:11]
	v_lshl_add_u64 v[18:19], v[10:11], 0, v[198:199]
	v_and_b32_e32 v11, 64, v226
	v_xor_b32_e32 v10, 1, v226
	v_add_u32_e32 v11, 64, v11
	v_cmp_lt_i32_e32 vcc, v10, v11
	v_lshl_add_u64 v[2:3], v[2:3], 0, v[212:213]
	global_load_dwordx4 v[2:5], v[2:3], off
	v_cndmask_b32_e32 v10, v226, v10, vcc
	v_lshlrev_b32_e32 v23, 2, v10
	v_xor_b32_e32 v10, 2, v226
	v_cmp_lt_i32_e32 vcc, v10, v11
	ds_read_b128 v[14:17], v24
	s_nop 0
	v_cndmask_b32_e32 v10, v226, v10, vcc
	v_lshlrev_b32_e32 v22, 2, v10
	v_xor_b32_e32 v10, 4, v226
	v_cmp_lt_i32_e32 vcc, v10, v11
	s_nop 1
	v_cndmask_b32_e32 v10, v226, v10, vcc
	v_lshlrev_b32_e32 v21, 2, v10
	v_xor_b32_e32 v10, 8, v226
	v_cmp_lt_i32_e32 vcc, v10, v11
	s_nop 1
	v_cndmask_b32_e32 v10, v226, v10, vcc
	v_lshlrev_b32_e32 v20, 2, v10
	ds_read_b128 v[10:13], v25
	s_waitcnt lgkmcnt(0)
	v_mul_f32_e32 v26, v11, v11
	v_mul_f32_e32 v27, v13, v13
	v_fmac_f32_e32 v26, v10, v10
	v_fmac_f32_e32 v27, v12, v12
	v_add_f32_e32 v26, v26, v27
	v_mul_f32_e32 v27, v15, v15
	v_fmac_f32_e32 v27, v14, v14
	v_add_f32_e32 v26, v26, v27
	v_mul_f32_e32 v27, v17, v17
	v_fmac_f32_e32 v27, v16, v16
	v_add_f32_e32 v26, v27, v26
	s_nop 1
	v_mov_b32_dpp v27, v26 quad_perm:[1,0,3,2] row_mask:0xf bank_mask:0xf
	s_waitcnt lgkmcnt(0)
	v_add_f32_e32 v26, v26, v27
	s_nop 1
	v_mov_b32_dpp v27, v26 quad_perm:[2,3,0,1] row_mask:0xf bank_mask:0xf
	s_waitcnt lgkmcnt(0)
	v_add_f32_e32 v26, v26, v27
	s_nop 1
	v_mov_b32_dpp v27, v26 row_half_mirror row_mask:0xf bank_mask:0xf
	s_waitcnt lgkmcnt(0)
	v_add_f32_e32 v26, v26, v27
	s_nop 1
	v_mov_b32_dpp v27, v26 row_mirror row_mask:0xf bank_mask:0xf
	s_waitcnt lgkmcnt(0)
	v_add_f32_e32 v26, v26, v27
	v_fmamk_f32 v26, v26, 0x3c000000, v232
	v_cmp_gt_f32_e32 vcc, s82, v26
	v_mul_f32_e32 v27, 0x4f800000, v26
	s_nop 0
	v_cndmask_b32_e32 v26, v26, v27, vcc
	v_sqrt_f32_e32 v27, v26
	s_nop 0
	v_add_u32_e32 v28, -1, v27
	v_fma_f32 v29, -v28, v27, v26
	v_cmp_ge_f32_e64 s[44:45], 0, v29
	v_add_u32_e32 v29, 1, v27
	s_nop 0
	v_cndmask_b32_e64 v28, v27, v28, s[44:45]
	v_fma_f32 v27, -v29, v27, v26
	v_cmp_lt_f32_e64 s[44:45], 0, v27
	s_nop 1
	v_cndmask_b32_e64 v27, v28, v29, s[44:45]
	v_mul_f32_e32 v28, 0x37800000, v27
	v_cndmask_b32_e32 v27, v27, v28, vcc
	v_cmp_class_f32_e32 vcc, v26, v229
	s_nop 1
	v_cndmask_b32_e32 v26, v27, v26, vcc
	v_div_scale_f32 v27, s[4:5], v26, v26, v237
	v_rcp_f32_e32 v28, v27
	s_nop 0
	v_fma_f32 v29, -v27, v28, 1.0
	v_fmac_f32_e32 v28, v29, v28
	v_div_scale_f32 v29, vcc, v237, v26, v237
	v_mul_f32_e32 v30, v29, v28
	v_fma_f32 v31, -v27, v30, v29
	v_fmac_f32_e32 v30, v31, v28
	v_fma_f32 v27, -v27, v30, v29
	v_div_fmas_f32 v27, v27, v28, v30
	v_div_fixup_f32 v26, v27, v26, v237
	v_mul_f32_e32 v10, v10, v26
	v_mul_f32_e32 v11, v11, v26
	s_waitcnt vmcnt(1)
	v_mul_f32_e32 v10, v6, v10
	v_mul_f32_e32 v11, v7, v11
	v_med3_f32 v10, v10, s33, v233
	v_med3_f32 v11, v11, s33, v233
	v_mov_b32_e32 v27, v1
	v_cvt_pk_fp8_f32 v27, v10, v11
	v_mul_f32_e32 v12, v12, v26
	v_mul_f32_e32 v13, v13, v26
	v_mul_f32_e32 v12, v8, v12
	v_mul_f32_e32 v13, v9, v13
	v_med3_f32 v10, v12, s33, v233
	v_med3_f32 v11, v13, s33, v233
	v_cvt_pk_fp8_f32 v27, v10, v11 op_sel:[0,0,1]
	v_mul_f32_e32 v10, v14, v26
	v_mul_f32_e32 v11, v15, v26
	s_waitcnt vmcnt(0)
	v_mul_f32_e32 v10, v2, v10
	v_mul_f32_e32 v11, v3, v11
	v_med3_f32 v10, v10, s33, v233
	v_med3_f32 v11, v11, s33, v233
	v_mov_b32_e32 v14, v1
	v_cvt_pk_fp8_f32 v14, v10, v11
	v_mul_f32_e32 v12, v16, v26
	v_mul_f32_e32 v13, v17, v26
	v_mul_f32_e32 v12, v4, v12
	v_mul_f32_e32 v13, v5, v13
	v_med3_f32 v10, v12, s33, v233
	v_med3_f32 v11, v13, s33, v233
	v_cvt_pk_fp8_f32 v14, v10, v11 op_sel:[0,0,1]
	s_nop 0
	v_cndmask_b32_e64 v10, v14, v27, s[42:43]
	v_cndmask_b32_e64 v11, v27, v14, s[42:43]
	global_store_dwordx2 v[18:19], v[10:11], off
	ds_read_b128 v[10:13], v25 offset:2048
	ds_read_b128 v[14:17], v24 offset:2048
	s_waitcnt lgkmcnt(1)
	v_mul_f32_e32 v26, v11, v11
	v_mul_f32_e32 v27, v13, v13
	v_fmac_f32_e32 v26, v10, v10
	v_fmac_f32_e32 v27, v12, v12
	v_add_f32_e32 v26, v26, v27
	s_waitcnt lgkmcnt(0)
	v_mul_f32_e32 v27, v15, v15
	v_fmac_f32_e32 v27, v14, v14
	v_add_f32_e32 v26, v26, v27
	v_mul_f32_e32 v27, v17, v17
	v_fmac_f32_e32 v27, v16, v16
	v_add_f32_e32 v26, v27, v26
	s_nop 1
	v_mov_b32_dpp v27, v26 quad_perm:[1,0,3,2] row_mask:0xf bank_mask:0xf
	s_waitcnt lgkmcnt(0)
	v_add_f32_e32 v26, v26, v27
	s_nop 1
	v_mov_b32_dpp v27, v26 quad_perm:[2,3,0,1] row_mask:0xf bank_mask:0xf
	s_waitcnt lgkmcnt(0)
	v_add_f32_e32 v26, v26, v27
	s_nop 1
	v_mov_b32_dpp v27, v26 row_half_mirror row_mask:0xf bank_mask:0xf
	s_waitcnt lgkmcnt(0)
	v_add_f32_e32 v26, v26, v27
	s_nop 1
	v_mov_b32_dpp v27, v26 row_mirror row_mask:0xf bank_mask:0xf
	s_waitcnt lgkmcnt(0)
	v_add_f32_e32 v26, v26, v27
	v_fmamk_f32 v26, v26, 0x3c000000, v232
	v_cmp_gt_f32_e32 vcc, s82, v26
	v_mul_f32_e32 v27, 0x4f800000, v26
	s_nop 0
	v_cndmask_b32_e32 v26, v26, v27, vcc
	v_sqrt_f32_e32 v27, v26
	s_nop 0
	v_add_u32_e32 v28, -1, v27
	v_fma_f32 v29, -v28, v27, v26
	v_cmp_ge_f32_e64 s[44:45], 0, v29
	v_add_u32_e32 v29, 1, v27
	s_nop 0
	v_cndmask_b32_e64 v28, v27, v28, s[44:45]
	v_fma_f32 v27, -v29, v27, v26
	v_cmp_lt_f32_e64 s[44:45], 0, v27
	s_nop 1
	v_cndmask_b32_e64 v27, v28, v29, s[44:45]
	v_mul_f32_e32 v28, 0x37800000, v27
	v_cndmask_b32_e32 v27, v27, v28, vcc
	v_cmp_class_f32_e32 vcc, v26, v229
	s_nop 1
	v_cndmask_b32_e32 v26, v27, v26, vcc
	v_div_scale_f32 v27, s[4:5], v26, v26, v237
	v_rcp_f32_e32 v28, v27
	s_movk_i32 s4, 0x2000
	v_fma_f32 v29, -v27, v28, 1.0
	v_fmac_f32_e32 v28, v29, v28
	v_div_scale_f32 v29, vcc, v237, v26, v237
	v_mul_f32_e32 v30, v29, v28
	v_fma_f32 v31, -v27, v30, v29
	v_fmac_f32_e32 v30, v31, v28
	v_fma_f32 v27, -v27, v30, v29
	v_div_fmas_f32 v27, v27, v28, v30
	v_div_fixup_f32 v26, v27, v26, v237
	v_mul_f32_e32 v10, v10, v26
	v_mul_f32_e32 v11, v11, v26
	v_mul_f32_e32 v10, v6, v10
	v_mul_f32_e32 v11, v7, v11
	v_med3_f32 v10, v10, s33, v233
	v_med3_f32 v11, v11, s33, v233
	v_mov_b32_e32 v27, v1
	v_cvt_pk_fp8_f32 v27, v10, v11
	v_mul_f32_e32 v12, v12, v26
	v_mul_f32_e32 v13, v13, v26
	v_mul_f32_e32 v12, v8, v12
	v_mul_f32_e32 v13, v9, v13
	v_med3_f32 v10, v12, s33, v233
	v_med3_f32 v11, v13, s33, v233
	v_cvt_pk_fp8_f32 v27, v10, v11 op_sel:[0,0,1]
	v_mul_f32_e32 v10, v14, v26
	v_mul_f32_e32 v11, v15, v26
	v_mul_f32_e32 v10, v2, v10
	v_mul_f32_e32 v11, v3, v11
	v_med3_f32 v10, v10, s33, v233
	v_med3_f32 v11, v11, s33, v233
	v_mov_b32_e32 v14, v1
	v_cvt_pk_fp8_f32 v14, v10, v11
	v_mul_f32_e32 v12, v16, v26
	v_mul_f32_e32 v13, v17, v26
	v_mul_f32_e32 v12, v4, v12
	v_mul_f32_e32 v13, v5, v13
	v_med3_f32 v10, v12, s33, v233
	v_med3_f32 v11, v13, s33, v233
	v_cvt_pk_fp8_f32 v14, v10, v11 op_sel:[0,0,1]
	v_add_co_u32_e32 v12, vcc, s4, v18
	v_cndmask_b32_e64 v10, v14, v27, s[42:43]
	v_cndmask_b32_e64 v11, v27, v14, s[42:43]
	v_addc_co_u32_e32 v13, vcc, 0, v19, vcc
	global_store_dwordx2 v[12:13], v[10:11], off
	ds_read_b128 v[10:13], v25 offset:4096
	ds_read_b128 v[14:17], v24 offset:4096
	s_waitcnt lgkmcnt(1)
	v_mul_f32_e32 v26, v11, v11
	v_mul_f32_e32 v27, v13, v13
	v_fmac_f32_e32 v26, v10, v10
	v_fmac_f32_e32 v27, v12, v12
	v_add_f32_e32 v26, v26, v27
	s_waitcnt lgkmcnt(0)
	v_mul_f32_e32 v27, v15, v15
	v_fmac_f32_e32 v27, v14, v14
	v_add_f32_e32 v26, v26, v27
	v_mul_f32_e32 v27, v17, v17
	v_fmac_f32_e32 v27, v16, v16
	v_add_f32_e32 v26, v27, v26
	s_nop 1
	v_mov_b32_dpp v27, v26 quad_perm:[1,0,3,2] row_mask:0xf bank_mask:0xf
	s_waitcnt lgkmcnt(0)
	v_add_f32_e32 v26, v26, v27
	s_nop 1
	v_mov_b32_dpp v27, v26 quad_perm:[2,3,0,1] row_mask:0xf bank_mask:0xf
	s_waitcnt lgkmcnt(0)
	v_add_f32_e32 v26, v26, v27
	s_nop 1
	v_mov_b32_dpp v27, v26 row_half_mirror row_mask:0xf bank_mask:0xf
	s_waitcnt lgkmcnt(0)
	v_add_f32_e32 v26, v26, v27
	s_nop 1
	v_mov_b32_dpp v27, v26 row_mirror row_mask:0xf bank_mask:0xf
	s_waitcnt lgkmcnt(0)
	v_add_f32_e32 v26, v26, v27
	v_fmamk_f32 v26, v26, 0x3c000000, v232
	v_cmp_gt_f32_e32 vcc, s82, v26
	v_mul_f32_e32 v27, 0x4f800000, v26
	s_nop 0
	v_cndmask_b32_e32 v26, v26, v27, vcc
	v_sqrt_f32_e32 v27, v26
	s_nop 0
	v_add_u32_e32 v28, -1, v27
	v_fma_f32 v29, -v28, v27, v26
	v_cmp_ge_f32_e64 s[44:45], 0, v29
	v_add_u32_e32 v29, 1, v27
	s_nop 0
	v_cndmask_b32_e64 v28, v27, v28, s[44:45]
	v_fma_f32 v27, -v29, v27, v26
	v_cmp_lt_f32_e64 s[44:45], 0, v27
	s_nop 1
	v_cndmask_b32_e64 v27, v28, v29, s[44:45]
	v_mul_f32_e32 v28, 0x37800000, v27
	v_cndmask_b32_e32 v27, v27, v28, vcc
	v_cmp_class_f32_e32 vcc, v26, v229
	s_nop 1
	v_cndmask_b32_e32 v26, v27, v26, vcc
	v_div_scale_f32 v27, s[4:5], v26, v26, v237
	v_rcp_f32_e32 v28, v27
	s_movk_i32 s4, 0x4000
	v_fma_f32 v29, -v27, v28, 1.0
	v_fmac_f32_e32 v28, v29, v28
	v_div_scale_f32 v29, vcc, v237, v26, v237
	v_mul_f32_e32 v30, v29, v28
	v_fma_f32 v31, -v27, v30, v29
	v_fmac_f32_e32 v30, v31, v28
	v_fma_f32 v27, -v27, v30, v29
	v_div_fmas_f32 v27, v27, v28, v30
	v_div_fixup_f32 v26, v27, v26, v237
	v_mul_f32_e32 v10, v10, v26
	v_mul_f32_e32 v11, v11, v26
	v_mul_f32_e32 v10, v6, v10
	v_mul_f32_e32 v11, v7, v11
	v_med3_f32 v10, v10, s33, v233
	v_med3_f32 v11, v11, s33, v233
	v_mov_b32_e32 v27, v1
	v_cvt_pk_fp8_f32 v27, v10, v11
	v_mul_f32_e32 v12, v12, v26
	v_mul_f32_e32 v13, v13, v26
	v_mul_f32_e32 v12, v8, v12
	v_mul_f32_e32 v13, v9, v13
	v_med3_f32 v10, v12, s33, v233
	v_med3_f32 v11, v13, s33, v233
	v_cvt_pk_fp8_f32 v27, v10, v11 op_sel:[0,0,1]
	v_mul_f32_e32 v10, v14, v26
	v_mul_f32_e32 v11, v15, v26
	v_mul_f32_e32 v10, v2, v10
	v_mul_f32_e32 v11, v3, v11
	v_med3_f32 v10, v10, s33, v233
	v_med3_f32 v11, v11, s33, v233
	v_mov_b32_e32 v14, v1
	v_cvt_pk_fp8_f32 v14, v10, v11
	v_mul_f32_e32 v12, v16, v26
	v_mul_f32_e32 v13, v17, v26
	v_mul_f32_e32 v12, v4, v12
	v_mul_f32_e32 v13, v5, v13
	v_med3_f32 v10, v12, s33, v233
	v_med3_f32 v11, v13, s33, v233
	v_cvt_pk_fp8_f32 v14, v10, v11 op_sel:[0,0,1]
	v_add_co_u32_e32 v12, vcc, s4, v18
	v_cndmask_b32_e64 v10, v14, v27, s[42:43]
	v_cndmask_b32_e64 v11, v27, v14, s[42:43]
	v_addc_co_u32_e32 v13, vcc, 0, v19, vcc
	global_store_dwordx2 v[12:13], v[10:11], off
	ds_read_b128 v[10:13], v25 offset:6144
	ds_read_b128 v[14:17], v24 offset:6144
	s_waitcnt lgkmcnt(1)
	v_mul_f32_e32 v26, v11, v11
	v_mul_f32_e32 v27, v13, v13
	v_fmac_f32_e32 v26, v10, v10
	v_fmac_f32_e32 v27, v12, v12
	v_add_f32_e32 v26, v26, v27
	s_waitcnt lgkmcnt(0)
	v_mul_f32_e32 v27, v15, v15
	v_fmac_f32_e32 v27, v14, v14
	v_add_f32_e32 v26, v26, v27
	v_mul_f32_e32 v27, v17, v17
	v_fmac_f32_e32 v27, v16, v16
	v_add_f32_e32 v26, v27, v26
	s_nop 1
	v_mov_b32_dpp v27, v26 quad_perm:[1,0,3,2] row_mask:0xf bank_mask:0xf
	s_waitcnt lgkmcnt(0)
	v_add_f32_e32 v26, v26, v27
	s_nop 1
	v_mov_b32_dpp v27, v26 quad_perm:[2,3,0,1] row_mask:0xf bank_mask:0xf
	s_waitcnt lgkmcnt(0)
	v_add_f32_e32 v26, v26, v27
	s_nop 1
	v_mov_b32_dpp v27, v26 row_half_mirror row_mask:0xf bank_mask:0xf
	s_waitcnt lgkmcnt(0)
	v_add_f32_e32 v26, v26, v27
	s_nop 1
	v_mov_b32_dpp v27, v26 row_mirror row_mask:0xf bank_mask:0xf
	s_waitcnt lgkmcnt(0)
	v_add_f32_e32 v26, v26, v27
	v_fmamk_f32 v26, v26, 0x3c000000, v232
	v_cmp_gt_f32_e32 vcc, s82, v26
	v_mul_f32_e32 v27, 0x4f800000, v26
	s_nop 0
	v_cndmask_b32_e32 v26, v26, v27, vcc
	v_sqrt_f32_e32 v27, v26
	s_nop 0
	v_add_u32_e32 v28, -1, v27
	v_fma_f32 v29, -v28, v27, v26
	v_cmp_ge_f32_e64 s[44:45], 0, v29
	v_add_u32_e32 v29, 1, v27
	s_nop 0
	v_cndmask_b32_e64 v28, v27, v28, s[44:45]
	v_fma_f32 v27, -v29, v27, v26
	v_cmp_lt_f32_e64 s[44:45], 0, v27
	s_nop 1
	v_cndmask_b32_e64 v27, v28, v29, s[44:45]
	v_mul_f32_e32 v28, 0x37800000, v27
	v_cndmask_b32_e32 v27, v27, v28, vcc
	v_cmp_class_f32_e32 vcc, v26, v229
	s_nop 1
	v_cndmask_b32_e32 v26, v27, v26, vcc
	v_div_scale_f32 v27, s[4:5], v26, v26, v237
	v_rcp_f32_e32 v28, v27
	s_movk_i32 s4, 0x6000
	v_fma_f32 v29, -v27, v28, 1.0
	v_fmac_f32_e32 v28, v29, v28
	v_div_scale_f32 v29, vcc, v237, v26, v237
	v_mul_f32_e32 v30, v29, v28
	v_fma_f32 v31, -v27, v30, v29
	v_fmac_f32_e32 v30, v31, v28
	v_fma_f32 v27, -v27, v30, v29
	v_div_fmas_f32 v27, v27, v28, v30
	v_div_fixup_f32 v26, v27, v26, v237
	v_mul_f32_e32 v10, v10, v26
	v_mul_f32_e32 v11, v11, v26
	v_mul_f32_e32 v10, v6, v10
	v_mul_f32_e32 v11, v7, v11
	v_med3_f32 v10, v10, s33, v233
	v_med3_f32 v11, v11, s33, v233
	v_mov_b32_e32 v27, v1
	v_cvt_pk_fp8_f32 v27, v10, v11
	v_mul_f32_e32 v12, v12, v26
	v_mul_f32_e32 v13, v13, v26
	v_mul_f32_e32 v12, v8, v12
	v_mul_f32_e32 v13, v9, v13
	v_med3_f32 v10, v12, s33, v233
	v_med3_f32 v11, v13, s33, v233
	v_cvt_pk_fp8_f32 v27, v10, v11 op_sel:[0,0,1]
	v_mul_f32_e32 v10, v14, v26
	v_mul_f32_e32 v11, v15, v26
	v_mul_f32_e32 v10, v2, v10
	v_mul_f32_e32 v11, v3, v11
	v_med3_f32 v10, v10, s33, v233
	v_med3_f32 v11, v11, s33, v233
	v_mov_b32_e32 v14, v1
	v_cvt_pk_fp8_f32 v14, v10, v11
	v_mul_f32_e32 v12, v16, v26
	v_mul_f32_e32 v13, v17, v26
	v_mul_f32_e32 v12, v4, v12
	v_mul_f32_e32 v13, v5, v13
	v_med3_f32 v10, v12, s33, v233
	v_med3_f32 v11, v13, s33, v233
	v_cvt_pk_fp8_f32 v14, v10, v11 op_sel:[0,0,1]
	v_add_co_u32_e32 v12, vcc, s4, v18
	v_cndmask_b32_e64 v10, v14, v27, s[42:43]
	v_cndmask_b32_e64 v11, v27, v14, s[42:43]
	v_addc_co_u32_e32 v13, vcc, 0, v19, vcc
	global_store_dwordx2 v[12:13], v[10:11], off
	ds_read_b128 v[10:13], v25 offset:8192
	ds_read_b128 v[14:17], v24 offset:8192
	s_waitcnt lgkmcnt(1)
	v_mul_f32_e32 v26, v11, v11
	v_mul_f32_e32 v27, v13, v13
	v_fmac_f32_e32 v26, v10, v10
	v_fmac_f32_e32 v27, v12, v12
	v_add_f32_e32 v26, v26, v27
	s_waitcnt lgkmcnt(0)
	v_mul_f32_e32 v27, v15, v15
	v_fmac_f32_e32 v27, v14, v14
	v_add_f32_e32 v26, v26, v27
	v_mul_f32_e32 v27, v17, v17
	v_fmac_f32_e32 v27, v16, v16
	v_add_f32_e32 v26, v27, v26
	s_nop 1
	v_mov_b32_dpp v27, v26 quad_perm:[1,0,3,2] row_mask:0xf bank_mask:0xf
	s_waitcnt lgkmcnt(0)
	v_add_f32_e32 v26, v26, v27
	s_nop 1
	v_mov_b32_dpp v27, v26 quad_perm:[2,3,0,1] row_mask:0xf bank_mask:0xf
	s_waitcnt lgkmcnt(0)
	v_add_f32_e32 v26, v26, v27
	s_nop 1
	v_mov_b32_dpp v27, v26 row_half_mirror row_mask:0xf bank_mask:0xf
	s_waitcnt lgkmcnt(0)
	v_add_f32_e32 v26, v26, v27
	s_nop 1
	v_mov_b32_dpp v27, v26 row_mirror row_mask:0xf bank_mask:0xf
	s_waitcnt lgkmcnt(0)
	v_add_f32_e32 v26, v26, v27
	v_fmamk_f32 v26, v26, 0x3c000000, v232
	v_cmp_gt_f32_e32 vcc, s82, v26
	v_mul_f32_e32 v27, 0x4f800000, v26
	s_nop 0
	v_cndmask_b32_e32 v26, v26, v27, vcc
	v_sqrt_f32_e32 v27, v26
	s_nop 0
	v_add_u32_e32 v28, -1, v27
	v_fma_f32 v29, -v28, v27, v26
	v_cmp_ge_f32_e64 s[44:45], 0, v29
	v_add_u32_e32 v29, 1, v27
	s_nop 0
	v_cndmask_b32_e64 v28, v27, v28, s[44:45]
	v_fma_f32 v27, -v29, v27, v26
	v_cmp_lt_f32_e64 s[44:45], 0, v27
	s_nop 1
	v_cndmask_b32_e64 v27, v28, v29, s[44:45]
	v_mul_f32_e32 v28, 0x37800000, v27
	v_cndmask_b32_e32 v27, v27, v28, vcc
	v_cmp_class_f32_e32 vcc, v26, v229
	s_nop 1
	v_cndmask_b32_e32 v26, v27, v26, vcc
	v_div_scale_f32 v27, s[4:5], v26, v26, v237
	v_rcp_f32_e32 v28, v27
	s_mov_b32 s4, 0x8000
	v_fma_f32 v29, -v27, v28, 1.0
	v_fmac_f32_e32 v28, v29, v28
	v_div_scale_f32 v29, vcc, v237, v26, v237
	v_mul_f32_e32 v30, v29, v28
	v_fma_f32 v31, -v27, v30, v29
	v_fmac_f32_e32 v30, v31, v28
	v_fma_f32 v27, -v27, v30, v29
	v_div_fmas_f32 v27, v27, v28, v30
	v_div_fixup_f32 v26, v27, v26, v237
	v_mul_f32_e32 v10, v10, v26
	v_mul_f32_e32 v11, v11, v26
	v_mul_f32_e32 v10, v6, v10
	v_mul_f32_e32 v11, v7, v11
	v_med3_f32 v10, v10, s33, v233
	v_med3_f32 v11, v11, s33, v233
	v_mov_b32_e32 v27, v1
	v_cvt_pk_fp8_f32 v27, v10, v11
	v_mul_f32_e32 v12, v12, v26
	v_mul_f32_e32 v13, v13, v26
	v_mul_f32_e32 v12, v8, v12
	v_mul_f32_e32 v13, v9, v13
	v_med3_f32 v10, v12, s33, v233
	v_med3_f32 v11, v13, s33, v233
	v_cvt_pk_fp8_f32 v27, v10, v11 op_sel:[0,0,1]
	v_mul_f32_e32 v10, v14, v26
	v_mul_f32_e32 v11, v15, v26
	v_mul_f32_e32 v10, v2, v10
	v_mul_f32_e32 v11, v3, v11
	v_med3_f32 v10, v10, s33, v233
	v_med3_f32 v11, v11, s33, v233
	v_mov_b32_e32 v14, v1
	v_cvt_pk_fp8_f32 v14, v10, v11
	v_mul_f32_e32 v12, v16, v26
	v_mul_f32_e32 v13, v17, v26
	v_mul_f32_e32 v12, v4, v12
	v_mul_f32_e32 v13, v5, v13
	v_med3_f32 v10, v12, s33, v233
	v_med3_f32 v11, v13, s33, v233
	v_cvt_pk_fp8_f32 v14, v10, v11 op_sel:[0,0,1]
	v_add_co_u32_e32 v12, vcc, s4, v18
	v_cndmask_b32_e64 v10, v14, v27, s[42:43]
	v_cndmask_b32_e64 v11, v27, v14, s[42:43]
	v_addc_co_u32_e32 v13, vcc, 0, v19, vcc
	global_store_dwordx2 v[12:13], v[10:11], off
	ds_read_b128 v[10:13], v25 offset:10240
	ds_read_b128 v[14:17], v24 offset:10240
	s_waitcnt lgkmcnt(1)
	v_mul_f32_e32 v26, v11, v11
	v_mul_f32_e32 v27, v13, v13
	v_fmac_f32_e32 v26, v10, v10
	v_fmac_f32_e32 v27, v12, v12
	v_add_f32_e32 v26, v26, v27
	s_waitcnt lgkmcnt(0)
	v_mul_f32_e32 v27, v15, v15
	v_fmac_f32_e32 v27, v14, v14
	v_add_f32_e32 v26, v26, v27
	v_mul_f32_e32 v27, v17, v17
	v_fmac_f32_e32 v27, v16, v16
	v_add_f32_e32 v26, v27, v26
	s_nop 1
	v_mov_b32_dpp v27, v26 quad_perm:[1,0,3,2] row_mask:0xf bank_mask:0xf
	s_waitcnt lgkmcnt(0)
	v_add_f32_e32 v26, v26, v27
	s_nop 1
	v_mov_b32_dpp v27, v26 quad_perm:[2,3,0,1] row_mask:0xf bank_mask:0xf
	s_waitcnt lgkmcnt(0)
	v_add_f32_e32 v26, v26, v27
	s_nop 1
	v_mov_b32_dpp v27, v26 row_half_mirror row_mask:0xf bank_mask:0xf
	s_waitcnt lgkmcnt(0)
	v_add_f32_e32 v26, v26, v27
	s_nop 1
	v_mov_b32_dpp v27, v26 row_mirror row_mask:0xf bank_mask:0xf
	s_waitcnt lgkmcnt(0)
	v_add_f32_e32 v26, v26, v27
	v_fmamk_f32 v26, v26, 0x3c000000, v232
	v_cmp_gt_f32_e32 vcc, s82, v26
	v_mul_f32_e32 v27, 0x4f800000, v26
	s_nop 0
	v_cndmask_b32_e32 v26, v26, v27, vcc
	v_sqrt_f32_e32 v27, v26
	s_nop 0
	v_add_u32_e32 v28, -1, v27
	v_fma_f32 v29, -v28, v27, v26
	v_cmp_ge_f32_e64 s[44:45], 0, v29
	v_add_u32_e32 v29, 1, v27
	s_nop 0
	v_cndmask_b32_e64 v28, v27, v28, s[44:45]
	v_fma_f32 v27, -v29, v27, v26
	v_cmp_lt_f32_e64 s[44:45], 0, v27
	s_nop 1
	v_cndmask_b32_e64 v27, v28, v29, s[44:45]
	v_mul_f32_e32 v28, 0x37800000, v27
	v_cndmask_b32_e32 v27, v27, v28, vcc
	v_cmp_class_f32_e32 vcc, v26, v229
	s_nop 1
	v_cndmask_b32_e32 v26, v27, v26, vcc
	v_div_scale_f32 v27, s[4:5], v26, v26, v237
	v_rcp_f32_e32 v28, v27
	s_mov_b32 s4, 0xa000
	v_fma_f32 v29, -v27, v28, 1.0
	v_fmac_f32_e32 v28, v29, v28
	v_div_scale_f32 v29, vcc, v237, v26, v237
	v_mul_f32_e32 v30, v29, v28
	v_fma_f32 v31, -v27, v30, v29
	v_fmac_f32_e32 v30, v31, v28
	v_fma_f32 v27, -v27, v30, v29
	v_div_fmas_f32 v27, v27, v28, v30
	v_div_fixup_f32 v26, v27, v26, v237
	v_mul_f32_e32 v10, v10, v26
	v_mul_f32_e32 v11, v11, v26
	v_mul_f32_e32 v10, v6, v10
	v_mul_f32_e32 v11, v7, v11
	v_med3_f32 v10, v10, s33, v233
	v_med3_f32 v11, v11, s33, v233
	v_mov_b32_e32 v27, v1
	v_cvt_pk_fp8_f32 v27, v10, v11
	v_mul_f32_e32 v12, v12, v26
	v_mul_f32_e32 v13, v13, v26
	v_mul_f32_e32 v12, v8, v12
	v_mul_f32_e32 v13, v9, v13
	v_med3_f32 v10, v12, s33, v233
	v_med3_f32 v11, v13, s33, v233
	v_cvt_pk_fp8_f32 v27, v10, v11 op_sel:[0,0,1]
	v_mul_f32_e32 v10, v14, v26
	v_mul_f32_e32 v11, v15, v26
	v_mul_f32_e32 v10, v2, v10
	v_mul_f32_e32 v11, v3, v11
	v_med3_f32 v10, v10, s33, v233
	v_med3_f32 v11, v11, s33, v233
	v_mov_b32_e32 v14, v1
	v_cvt_pk_fp8_f32 v14, v10, v11
	v_mul_f32_e32 v12, v16, v26
	v_mul_f32_e32 v13, v17, v26
	v_mul_f32_e32 v12, v4, v12
	v_mul_f32_e32 v13, v5, v13
	v_med3_f32 v10, v12, s33, v233
	v_med3_f32 v11, v13, s33, v233
	v_cvt_pk_fp8_f32 v14, v10, v11 op_sel:[0,0,1]
	v_add_co_u32_e32 v12, vcc, s4, v18
	v_cndmask_b32_e64 v10, v14, v27, s[42:43]
	v_cndmask_b32_e64 v11, v27, v14, s[42:43]
	v_addc_co_u32_e32 v13, vcc, 0, v19, vcc
	global_store_dwordx2 v[12:13], v[10:11], off
	ds_read_b128 v[10:13], v25 offset:12288
	ds_read_b128 v[14:17], v24 offset:12288
	s_waitcnt lgkmcnt(1)
	v_mul_f32_e32 v26, v11, v11
	v_mul_f32_e32 v27, v13, v13
	v_fmac_f32_e32 v26, v10, v10
	v_fmac_f32_e32 v27, v12, v12
	v_add_f32_e32 v26, v26, v27
	s_waitcnt lgkmcnt(0)
	v_mul_f32_e32 v27, v15, v15
	v_fmac_f32_e32 v27, v14, v14
	v_add_f32_e32 v26, v26, v27
	v_mul_f32_e32 v27, v17, v17
	v_fmac_f32_e32 v27, v16, v16
	v_add_f32_e32 v26, v27, v26
	s_nop 1
	v_mov_b32_dpp v27, v26 quad_perm:[1,0,3,2] row_mask:0xf bank_mask:0xf
	s_waitcnt lgkmcnt(0)
	v_add_f32_e32 v26, v26, v27
	s_nop 1
	v_mov_b32_dpp v27, v26 quad_perm:[2,3,0,1] row_mask:0xf bank_mask:0xf
	s_waitcnt lgkmcnt(0)
	v_add_f32_e32 v26, v26, v27
	s_nop 1
	v_mov_b32_dpp v27, v26 row_half_mirror row_mask:0xf bank_mask:0xf
	s_waitcnt lgkmcnt(0)
	v_add_f32_e32 v26, v26, v27
	s_nop 1
	v_mov_b32_dpp v27, v26 row_mirror row_mask:0xf bank_mask:0xf
	s_waitcnt lgkmcnt(0)
	v_add_f32_e32 v26, v26, v27
	v_fmamk_f32 v26, v26, 0x3c000000, v232
	v_cmp_gt_f32_e32 vcc, s82, v26
	v_mul_f32_e32 v27, 0x4f800000, v26
	s_nop 0
	v_cndmask_b32_e32 v26, v26, v27, vcc
	v_sqrt_f32_e32 v27, v26
	s_nop 0
	v_add_u32_e32 v28, -1, v27
	v_fma_f32 v29, -v28, v27, v26
	v_cmp_ge_f32_e64 s[44:45], 0, v29
	v_add_u32_e32 v29, 1, v27
	s_nop 0
	v_cndmask_b32_e64 v28, v27, v28, s[44:45]
	v_fma_f32 v27, -v29, v27, v26
	v_cmp_lt_f32_e64 s[44:45], 0, v27
	s_nop 1
	v_cndmask_b32_e64 v27, v28, v29, s[44:45]
	v_mul_f32_e32 v28, 0x37800000, v27
	v_cndmask_b32_e32 v27, v27, v28, vcc
	v_cmp_class_f32_e32 vcc, v26, v229
	s_nop 1
	v_cndmask_b32_e32 v26, v27, v26, vcc
	v_div_scale_f32 v27, s[4:5], v26, v26, v237
	v_rcp_f32_e32 v28, v27
	s_mov_b32 s4, 0xc000
	v_fma_f32 v29, -v27, v28, 1.0
	v_fmac_f32_e32 v28, v29, v28
	v_div_scale_f32 v29, vcc, v237, v26, v237
	v_mul_f32_e32 v30, v29, v28
	v_fma_f32 v31, -v27, v30, v29
	v_fmac_f32_e32 v30, v31, v28
	v_fma_f32 v27, -v27, v30, v29
	v_div_fmas_f32 v27, v27, v28, v30
	v_div_fixup_f32 v26, v27, v26, v237
	v_mul_f32_e32 v10, v10, v26
	v_mul_f32_e32 v11, v11, v26
	v_mul_f32_e32 v10, v6, v10
	v_mul_f32_e32 v11, v7, v11
	v_med3_f32 v10, v10, s33, v233
	v_med3_f32 v11, v11, s33, v233
	v_mov_b32_e32 v27, v1
	v_cvt_pk_fp8_f32 v27, v10, v11
	v_mul_f32_e32 v12, v12, v26
	v_mul_f32_e32 v13, v13, v26
	v_mul_f32_e32 v12, v8, v12
	v_mul_f32_e32 v13, v9, v13
	v_med3_f32 v10, v12, s33, v233
	v_med3_f32 v11, v13, s33, v233
	v_cvt_pk_fp8_f32 v27, v10, v11 op_sel:[0,0,1]
	v_mul_f32_e32 v10, v14, v26
	v_mul_f32_e32 v11, v15, v26
	v_mul_f32_e32 v10, v2, v10
	v_mul_f32_e32 v11, v3, v11
	v_med3_f32 v10, v10, s33, v233
	v_med3_f32 v11, v11, s33, v233
	v_mov_b32_e32 v14, v1
	v_cvt_pk_fp8_f32 v14, v10, v11
	v_mul_f32_e32 v12, v16, v26
	v_mul_f32_e32 v13, v17, v26
	v_mul_f32_e32 v12, v4, v12
	v_mul_f32_e32 v13, v5, v13
	v_med3_f32 v10, v12, s33, v233
	v_med3_f32 v11, v13, s33, v233
	v_cvt_pk_fp8_f32 v14, v10, v11 op_sel:[0,0,1]
	v_add_co_u32_e32 v12, vcc, s4, v18
	v_cndmask_b32_e64 v10, v14, v27, s[42:43]
	v_cndmask_b32_e64 v11, v27, v14, s[42:43]
	v_addc_co_u32_e32 v13, vcc, 0, v19, vcc
	global_store_dwordx2 v[12:13], v[10:11], off
	ds_read_b128 v[14:17], v25 offset:14336
	ds_read_b128 v[10:13], v24 offset:14336
	s_waitcnt lgkmcnt(1)
	v_mul_f32_e32 v24, v15, v15
	v_mul_f32_e32 v25, v17, v17
	v_fmac_f32_e32 v24, v14, v14
	v_fmac_f32_e32 v25, v16, v16
	v_add_f32_e32 v24, v24, v25
	s_waitcnt lgkmcnt(0)
	v_mul_f32_e32 v25, v11, v11
	v_fmac_f32_e32 v25, v10, v10
	v_add_f32_e32 v24, v24, v25
	v_mul_f32_e32 v25, v13, v13
	v_fmac_f32_e32 v25, v12, v12
	v_add_f32_e32 v24, v25, v24
	s_nop 1
	v_mov_b32_dpp v23, v24 quad_perm:[1,0,3,2] row_mask:0xf bank_mask:0xf
	s_waitcnt lgkmcnt(0)
	v_add_f32_e32 v23, v24, v23
	s_nop 1
	v_mov_b32_dpp v22, v23 quad_perm:[2,3,0,1] row_mask:0xf bank_mask:0xf
	s_waitcnt lgkmcnt(0)
	v_add_f32_e32 v22, v23, v22
	s_nop 1
	v_mov_b32_dpp v21, v22 row_half_mirror row_mask:0xf bank_mask:0xf
	s_waitcnt lgkmcnt(0)
	v_add_f32_e32 v21, v22, v21
	s_nop 1
	v_mov_b32_dpp v20, v21 row_mirror row_mask:0xf bank_mask:0xf
	s_waitcnt lgkmcnt(0)
	v_add_f32_e32 v20, v21, v20
	v_fmamk_f32 v20, v20, 0x3c000000, v232
	v_cmp_gt_f32_e32 vcc, s82, v20
	v_mul_f32_e32 v21, 0x4f800000, v20
	s_nop 0
	v_cndmask_b32_e32 v20, v20, v21, vcc
	v_sqrt_f32_e32 v21, v20
	s_nop 0
	v_add_u32_e32 v22, -1, v21
	v_fma_f32 v23, -v22, v21, v20
	v_cmp_ge_f32_e64 s[44:45], 0, v23
	v_add_u32_e32 v23, 1, v21
	s_nop 0
	v_cndmask_b32_e64 v22, v21, v22, s[44:45]
	v_fma_f32 v21, -v23, v21, v20
	v_cmp_lt_f32_e64 s[44:45], 0, v21
	s_nop 1
	v_cndmask_b32_e64 v21, v22, v23, s[44:45]
	v_mul_f32_e32 v22, 0x37800000, v21
	v_cndmask_b32_e32 v21, v21, v22, vcc
	v_cmp_class_f32_e32 vcc, v20, v229
	s_nop 1
	v_cndmask_b32_e32 v20, v21, v20, vcc
	v_div_scale_f32 v21, s[4:5], v20, v20, v237
	v_rcp_f32_e32 v22, v21
	s_nop 0
	v_fma_f32 v23, -v21, v22, 1.0
	v_fmac_f32_e32 v22, v23, v22
	v_div_scale_f32 v23, vcc, v237, v20, v237
	v_mul_f32_e32 v24, v23, v22
	v_fma_f32 v25, -v21, v24, v23
	v_fmac_f32_e32 v24, v25, v22
	v_fma_f32 v21, -v21, v24, v23
	v_div_fmas_f32 v21, v21, v22, v24
	v_div_fixup_f32 v20, v21, v20, v237
	v_mul_f32_e32 v14, v14, v20
	v_mul_f32_e32 v6, v6, v14
	v_mul_f32_e32 v14, v15, v20
	v_mul_f32_e32 v7, v7, v14
	v_mul_f32_e32 v14, v16, v20
	v_mul_f32_e32 v8, v8, v14
	v_mul_f32_e32 v14, v17, v20
	v_mul_f32_e32 v9, v9, v14
	v_med3_f32 v6, v6, s33, v233
	v_med3_f32 v7, v7, s33, v233
	v_mov_b32_e32 v14, v1
	v_cvt_pk_fp8_f32 v14, v6, v7
	v_med3_f32 v6, v8, s33, v233
	v_med3_f32 v7, v9, s33, v233
	v_cvt_pk_fp8_f32 v14, v6, v7 op_sel:[0,0,1]
	v_mul_f32_e32 v6, v10, v20
	v_mul_f32_e32 v2, v2, v6
	v_mul_f32_e32 v6, v11, v20
	v_mul_f32_e32 v3, v3, v6
	v_mul_f32_e32 v6, v12, v20
	v_mul_f32_e32 v4, v4, v6
	v_mul_f32_e32 v6, v13, v20
	v_mul_f32_e32 v5, v5, v6
	v_med3_f32 v2, v2, s33, v233
	v_med3_f32 v3, v3, s33, v233
	v_mov_b32_e32 v6, v1
	v_cvt_pk_fp8_f32 v6, v2, v3
	v_med3_f32 v2, v4, s33, v233
	v_med3_f32 v3, v5, s33, v233
	v_add_co_u32_e32 v4, vcc, 0xe000, v18
	v_cvt_pk_fp8_f32 v6, v2, v3 op_sel:[0,0,1]
	s_nop 0
	v_addc_co_u32_e32 v5, vcc, 0, v19, vcc
	v_cndmask_b32_e64 v2, v6, v14, s[42:43]
	v_cndmask_b32_e64 v3, v14, v6, s[42:43]
	global_store_dwordx2 v[4:5], v[2:3], off
	s_branch .LBB0_1020
